# static s_setprio 1 for waves 0-3 at kernel entry (mirror of previous)
# speedup vs baseline: 1.0118x; 1.0047x over previous
; __device__ __forceinline__ int lane_id() { unsigned z = 0u; asm volatile("" : "+v"(z)); return (int)__builtin_amdgcn_mbcnt_hi(~0u, __builtin_amdgcn_mbcnt_lo(~0u, z)); }
; __global__ void __launch_bounds__(NTHR, 2) mk_fwd(Args args) {
;     ...
;     c.wave = __builtin_amdgcn_readfirstlane((int)threadIdx.x >> 6); c.lane = lane_id(); c.tid = c.wave * 64 + c.lane;     c.G = gridDim.x; c.bid = blockIdx.x;
.LBB0_7:
	v_readlane_b32 s0, v254, 4
	s_lshr_b32 s0, s0, 6
	s_cmp_lt_u32 s0, 4
	s_cbranch_scc0 .Lprio_skip
	s_setprio 1
